# P8 epilogue: residual x loads (once-read f32) with nt policy
# speedup vs baseline: 1.0192x; 1.0043x over previous
; __device__ __forceinline__ int fresh_lane() { int l; asm volatile("v_mbcnt_lo_u32_b32 %0, -1, 0\n\tv_mbcnt_hi_u32_b32 %0, -1, %0" : "=v"(l)); return l; }
; __device__ __forceinline__ unsigned cvt_pk_bf16(float lo, float hi) { unsigned r; asm volatile("v_cvt_pk_bf16_f32 %0, %1, %2" : "=v"(r) : "v"(lo), "v"(hi)); return r; }
;     __device__ __forceinline__ void operator()(const f32x4 (&acc)[2][2][4][2], const Unit& u, int wr, int wc, int fr_, int fq_) const {
;         const int l_ = fresh_lane(), fr = l_ & 15, fq = l_ >> 4;
;         const int row0 = u.pm * BM + wr * 64 + fr, col0 = u.pn * BM + wc * 32 + 4 * fq;
; #pragma unroll
;         for (int ai = 0; ai < 2; ++ai)
; #pragma unroll
;             for (int m = 0; m < 4; ++m) { const size_t r = (size_t)(row0 + ai * HALF + m * 16); float ss = 0.f;
; #pragma unroll
;                 for (int bj = 0; bj < 2; ++bj)
; #pragma unroll
;                     for (int n = 0; n < 2; ++n) { const size_t o = r * ldc + col0 + bj * HALF + n * 16; const f32x4 c = *(const f32x4*)(R + o) + acc[ai][bj][m][n];
;                         ss += (c[0] * c[0] + c[1] * c[1]) + (c[2] * c[2] + c[3] * c[3]);
;                         u32x2 w; w.x = cvt_pk_bf16(c[0], c[1]); w.y = cvt_pk_bf16(c[2], c[3]); *(u32x2*)(HB + o) = w; }
;                 ss += __builtin_bit_cast(float, __builtin_amdgcn_ds_bpermute((l_ ^ 16) << 2, __builtin_bit_cast(int, ss)));
;                 ss += __builtin_bit_cast(float, __builtin_amdgcn_ds_bpermute((l_ ^ 32) << 2, __builtin_bit_cast(int, ss)));
;                 if (fq == 0) PSQ[r * 64 + u.pn * 4 + wc] = ss;
;                 asm volatile("" ::: "memory"); }
.LBB0_3067:
	s_lshl_b32 s41, s48, 8
	s_add_i32 s41, s41, s67
	v_mbcnt_lo_u32_b32 v158, -1, 0
	v_mbcnt_hi_u32_b32 v158, -1, v158
	s_lshl_b32 s48, s12, 2
	v_and_or_b32 v140, v158, 15, s41
	s_lshl_b32 s41, s12, 8
	v_ashrrev_i32_e32 v134, 2, v158
	s_or_b32 s41, s41, s70
	v_and_b32_e32 v134, -4, v134
	v_add_u32_e32 v138, s41, v134
	v_ashrrev_i32_e32 v141, 31, v140
	v_ashrrev_i32_e32 v139, 31, v138
	v_lshlrev_b64 v[134:135], 12, v[140:141]
	v_lshl_add_u64 v[136:137], v[134:135], 0, v[138:139]
	v_lshl_add_u64 v[150:151], v[136:137], 2, s[36:37]
	global_load_dwordx4 v[146:149], v[150:151], off nt
	v_lshl_add_u64 v[136:137], v[136:137], 1, s[14:15]
	v_cmp_gt_u32_e32 vcc, 16, v158
	s_ashr_i32 s49, s48, 31
	s_waitcnt vmcnt(0)
	v_pk_add_f32 v[128:129], v[128:129], v[148:149]
	v_pk_add_f32 v[152:153], v[126:127], v[146:147]
	s_nop 0
	v_cvt_pk_bf16_f32 v126, v152, v153
	v_cvt_pk_bf16_f32 v127, v128, v129
	global_store_dwordx2 v[136:137], v[126:127], off
	global_load_dwordx4 v[146:149], v[150:151], off offset:64 nt
	v_lshl_add_u64 v[126:127], v[138:139], 0, 16
	v_lshl_add_u64 v[136:137], v[126:127], 0, v[134:135]
	v_lshl_add_u64 v[136:137], v[136:137], 1, s[14:15]
	v_mul_f32_e32 v129, v129, v129
	v_fmac_f32_e32 v129, v128, v128
	s_waitcnt vmcnt(0)
	v_pk_add_f32 v[124:125], v[124:125], v[148:149]
	v_pk_add_f32 v[154:155], v[122:123], v[146:147]
	s_nop 0
	v_cvt_pk_bf16_f32 v122, v154, v155
	v_cvt_pk_bf16_f32 v123, v124, v125
	global_store_dwordx2 v[136:137], v[122:123], off
	global_load_dwordx4 v[146:149], v[150:151], off offset:512 nt
	v_lshl_add_u64 v[122:123], v[138:139], 0, s[18:19]
	v_lshl_add_u64 v[136:137], v[122:123], 0, v[134:135]
	v_lshl_add_u64 v[136:137], v[136:137], 1, s[14:15]
	v_mul_f32_e32 v125, v125, v125
	v_fmac_f32_e32 v125, v124, v124
	s_waitcnt vmcnt(0)
	v_pk_add_f32 v[120:121], v[120:121], v[148:149]
	v_pk_add_f32 v[156:157], v[118:119], v[146:147]
	s_nop 0
	v_cvt_pk_bf16_f32 v118, v156, v157
	v_cvt_pk_bf16_f32 v119, v120, v121
	global_store_dwordx2 v[136:137], v[118:119], off
	global_load_dwordx4 v[146:149], v[150:151], off offset:576 nt
	v_mul_f32_e32 v136, v153, v153
	v_fmac_f32_e32 v136, v152, v152
	v_add_f32_e32 v128, v136, v129
	v_mul_f32_e32 v129, v155, v155
	v_fmac_f32_e32 v129, v154, v154
	v_add_f32_e32 v124, v129, v125
	v_mul_f32_e32 v125, v157, v157
	v_mul_f32_e32 v121, v121, v121
	v_fmac_f32_e32 v125, v156, v156
	v_fmac_f32_e32 v121, v120, v120
	v_add_f32_e32 v124, v128, v124
	v_add_f32_e32 v120, v125, v121
	v_add_f32_e32 v128, v124, v120
	v_lshlrev_b32_e32 v118, 2, v158
	v_xor_b32_e32 v119, 64, v118
	v_xor_b32_e32 v118, 0x80, v118
	s_waitcnt vmcnt(0)
	v_pk_add_f32 v[120:121], v[116:117], v[148:149]
	v_pk_add_f32 v[124:125], v[114:115], v[146:147]
	v_mul_f32_e32 v115, v121, v121
	v_mul_f32_e32 v114, v125, v125
	v_fmac_f32_e32 v114, v124, v124
	v_fmac_f32_e32 v115, v120, v120
	v_add_f32_e32 v114, v114, v115
	v_add_f32_e32 v116, v128, v114
	ds_bpermute_b32 v117, v119, v116
	v_lshl_add_u64 v[114:115], v[138:139], 0, s[38:39]
	v_lshl_add_u64 v[128:129], v[114:115], 0, v[134:135]
	v_cvt_pk_bf16_f32 v124, v124, v125
	v_cvt_pk_bf16_f32 v125, v120, v121
	s_waitcnt lgkmcnt(0)
	v_add_f32_e32 v116, v116, v117
	ds_bpermute_b32 v117, v118, v116
	v_lshl_add_u64 v[120:121], v[128:129], 1, s[14:15]
	global_store_dwordx2 v[120:121], v[124:125], off
	s_and_saveexec_b64 s[50:51], vcc
	s_cbranch_execz .LBB0_3069
	v_lshlrev_b64 v[120:121], 8, v[140:141]
	v_lshl_add_u64 v[120:121], s[16:17], 0, v[120:121]
	v_lshl_add_u64 v[120:121], s[48:49], 2, v[120:121]
	s_lshl_b32 s12, s66, 2
	v_lshl_add_u64 v[120:121], v[120:121], 0, s[12:13]
	s_waitcnt lgkmcnt(0)
	v_add_f32_e32 v116, v116, v117
	global_store_dword v[120:121], v116, off
.LBB0_3069:
	s_or_b64 exec, exec, s[50:51]
	v_or_b32_e32 v116, 16, v140
	s_waitcnt lgkmcnt(0)
	v_ashrrev_i32_e32 v117, 31, v116
	v_lshlrev_b64 v[120:121], 12, v[116:117]
	v_lshl_add_u64 v[124:125], v[120:121], 0, v[138:139]
	v_lshl_add_u64 v[128:129], v[124:125], 2, s[36:37]
	global_load_dwordx4 v[146:149], v[128:129], off nt
	v_lshl_add_u64 v[124:125], v[124:125], 1, s[14:15]
	s_waitcnt vmcnt(0)
	v_pk_add_f32 v[134:135], v[112:113], v[148:149]
	v_pk_add_f32 v[136:137], v[110:111], v[146:147]
	s_nop 0
	v_cvt_pk_bf16_f32 v110, v136, v137
	v_cvt_pk_bf16_f32 v111, v134, v135
	global_store_dwordx2 v[124:125], v[110:111], off
	global_load_dwordx4 v[110:113], v[128:129], off offset:64 nt
	v_lshl_add_u64 v[124:125], v[120:121], 0, v[126:127]
	v_lshl_add_u64 v[124:125], v[124:125], 1, s[14:15]
	s_waitcnt vmcnt(0)
	v_pk_add_f32 v[112:113], v[108:109], v[112:113]
	v_pk_add_f32 v[110:111], v[106:107], v[110:111]
	s_nop 0
	v_cvt_pk_bf16_f32 v106, v110, v111
	v_cvt_pk_bf16_f32 v107, v112, v113
	global_store_dwordx2 v[124:125], v[106:107], off
	global_load_dwordx4 v[106:109], v[128:129], off offset:512 nt
	v_lshl_add_u64 v[124:125], v[120:121], 0, v[122:123]
	v_lshl_add_u64 v[124:125], v[124:125], 1, s[14:15]
	v_mul_f32_e32 v111, v111, v111
	v_mul_f32_e32 v113, v113, v113
	v_fmac_f32_e32 v111, v110, v110
	v_fmac_f32_e32 v113, v112, v112
	v_add_f32_e32 v110, v111, v113
	s_waitcnt vmcnt(0)
	v_pk_add_f32 v[108:109], v[104:105], v[108:109]
	v_pk_add_f32 v[106:107], v[102:103], v[106:107]
	s_nop 0
	v_cvt_pk_bf16_f32 v102, v106, v107
	v_cvt_pk_bf16_f32 v103, v108, v109
	global_store_dwordx2 v[124:125], v[102:103], off
	global_load_dwordx4 v[102:105], v[128:129], off offset:576 nt
	v_mul_f32_e32 v124, v137, v137
	v_mul_f32_e32 v125, v135, v135
	v_fmac_f32_e32 v124, v136, v136
	v_fmac_f32_e32 v125, v134, v134
	v_mul_f32_e32 v107, v107, v107
	v_mul_f32_e32 v109, v109, v109
	v_add_f32_e32 v124, v124, v125
	v_fmac_f32_e32 v107, v106, v106
	v_fmac_f32_e32 v109, v108, v108
	v_add_f32_e32 v110, v124, v110
	v_add_f32_e32 v106, v107, v109
	v_add_f32_e32 v106, v110, v106
	s_waitcnt vmcnt(0)
	v_pk_add_f32 v[100:101], v[100:101], v[104:105]
	v_pk_add_f32 v[102:103], v[98:99], v[102:103]
	v_mul_f32_e32 v99, v101, v101
	v_mul_f32_e32 v98, v103, v103
	v_fmac_f32_e32 v98, v102, v102
	v_fmac_f32_e32 v99, v100, v100
	v_add_f32_e32 v98, v98, v99
	v_add_f32_e32 v98, v106, v98
	ds_bpermute_b32 v99, v119, v98
	v_lshl_add_u64 v[104:105], v[120:121], 0, v[114:115]
	v_cvt_pk_bf16_f32 v102, v102, v103
	v_cvt_pk_bf16_f32 v103, v100, v101
	v_lshl_add_u64 v[100:101], v[104:105], 1, s[14:15]
	s_waitcnt lgkmcnt(0)
	v_add_f32_e32 v98, v98, v99
	ds_bpermute_b32 v99, v118, v98
	global_store_dwordx2 v[100:101], v[102:103], off
	s_and_saveexec_b64 s[50:51], vcc
	s_cbranch_execz .LBB0_3071
	v_lshlrev_b64 v[100:101], 8, v[116:117]
	v_lshl_add_u64 v[100:101], s[16:17], 0, v[100:101]
	v_lshl_add_u64 v[100:101], s[48:49], 2, v[100:101]
	s_lshl_b32 s12, s66, 2
	v_lshl_add_u64 v[100:101], v[100:101], 0, s[12:13]
	s_waitcnt lgkmcnt(0)
	v_add_f32_e32 v98, v98, v99
	global_store_dword v[100:101], v98, off
; __device__ __forceinline__ int fresh_lane() { int l; asm volatile("v_mbcnt_lo_u32_b32 %0, -1, 0\n\tv_mbcnt_hi_u32_b32 %0, -1, %0" : "=v"(l)); return l; }
; __device__ __forceinline__ unsigned cvt_pk_bf16(float lo, float hi) { unsigned r; asm volatile("v_cvt_pk_bf16_f32 %0, %1, %2" : "=v"(r) : "v"(lo), "v"(hi)); return r; }
;     __device__ __forceinline__ void operator()(const f32x4 (&acc)[2][2][4][2], const Unit& u, int wr, int wc, int fr_, int fq_) const {
;         const int l_ = fresh_lane(), fr = l_ & 15, fq = l_ >> 4;
;         const int row0 = u.pm * BM + wr * 64 + fr, col0 = u.pn * BM + wc * 32 + 4 * fq;
; #pragma unroll
;         for (int ai = 0; ai < 2; ++ai)
; #pragma unroll
;             for (int m = 0; m < 4; ++m) { const size_t r = (size_t)(row0 + ai * HALF + m * 16); float ss = 0.f;
; #pragma unroll
;                 for (int bj = 0; bj < 2; ++bj)
; #pragma unroll
;                     for (int n = 0; n < 2; ++n) { const size_t o = r * ldc + col0 + bj * HALF + n * 16; const f32x4 c = *(const f32x4*)(R + o) + acc[ai][bj][m][n];
;                         ss += (c[0] * c[0] + c[1] * c[1]) + (c[2] * c[2] + c[3] * c[3]);
;                         u32x2 w; w.x = cvt_pk_bf16(c[0], c[1]); w.y = cvt_pk_bf16(c[2], c[3]); *(u32x2*)(HB + o) = w; }
;                 ss += __builtin_bit_cast(float, __builtin_amdgcn_ds_bpermute((l_ ^ 16) << 2, __builtin_bit_cast(int, ss)));
;                 ss += __builtin_bit_cast(float, __builtin_amdgcn_ds_bpermute((l_ ^ 32) << 2, __builtin_bit_cast(int, ss)));
;                 if (fq == 0) PSQ[r * 64 + u.pn * 4 + wc] = ss;
;                 asm volatile("" ::: "memory"); }
.LBB0_3071:
	s_or_b64 exec, exec, s[50:51]
	v_or_b32_e32 v98, 32, v140
	s_waitcnt lgkmcnt(0)
	v_ashrrev_i32_e32 v99, 31, v98
	v_lshlrev_b64 v[104:105], 12, v[98:99]
	v_lshl_add_u64 v[106:107], v[104:105], 0, v[138:139]
	v_lshl_add_u64 v[108:109], v[106:107], 2, s[36:37]
	global_load_dwordx4 v[100:103], v[108:109], off nt
	v_lshl_add_u64 v[106:107], v[106:107], 1, s[14:15]
	s_waitcnt vmcnt(0)
	v_pk_add_f32 v[102:103], v[96:97], v[102:103]
	v_pk_add_f32 v[100:101], v[94:95], v[100:101]
	s_nop 0
	v_cvt_pk_bf16_f32 v94, v100, v101
	v_cvt_pk_bf16_f32 v95, v102, v103
	global_store_dwordx2 v[106:107], v[94:95], off
	global_load_dwordx4 v[94:97], v[108:109], off offset:64 nt
	v_lshl_add_u64 v[106:107], v[104:105], 0, v[126:127]
	v_lshl_add_u64 v[106:107], v[106:107], 1, s[14:15]
	v_mul_f32_e32 v101, v101, v101
	v_mul_f32_e32 v103, v103, v103
	v_fmac_f32_e32 v101, v100, v100
	v_fmac_f32_e32 v103, v102, v102
	v_add_f32_e32 v100, v101, v103
	s_waitcnt vmcnt(0)
	v_pk_add_f32 v[96:97], v[92:93], v[96:97]
	v_pk_add_f32 v[94:95], v[90:91], v[94:95]
	s_nop 0
	v_cvt_pk_bf16_f32 v90, v94, v95
	v_cvt_pk_bf16_f32 v91, v96, v97
	global_store_dwordx2 v[106:107], v[90:91], off
	global_load_dwordx4 v[90:93], v[108:109], off offset:512 nt
	v_lshl_add_u64 v[106:107], v[104:105], 0, v[122:123]
	v_lshl_add_u64 v[106:107], v[106:107], 1, s[14:15]
	v_mul_f32_e32 v95, v95, v95
	v_mul_f32_e32 v97, v97, v97
	v_fmac_f32_e32 v95, v94, v94
	v_fmac_f32_e32 v97, v96, v96
	v_add_f32_e32 v94, v95, v97
	v_add_f32_e32 v94, v100, v94
	s_waitcnt vmcnt(0)
	v_pk_add_f32 v[92:93], v[88:89], v[92:93]
	v_pk_add_f32 v[90:91], v[86:87], v[90:91]
	s_nop 0
	v_cvt_pk_bf16_f32 v86, v90, v91
	v_cvt_pk_bf16_f32 v87, v92, v93
	global_store_dwordx2 v[106:107], v[86:87], off
	global_load_dwordx4 v[86:89], v[108:109], off offset:576 nt
	v_mul_f32_e32 v91, v91, v91
	v_mul_f32_e32 v93, v93, v93
	v_fmac_f32_e32 v91, v90, v90
	v_fmac_f32_e32 v93, v92, v92
	v_add_f32_e32 v90, v91, v93
	v_add_f32_e32 v90, v94, v90
	s_waitcnt vmcnt(0)
	v_pk_add_f32 v[84:85], v[84:85], v[88:89]
	v_pk_add_f32 v[86:87], v[82:83], v[86:87]
	v_mul_f32_e32 v83, v85, v85
	v_mul_f32_e32 v82, v87, v87
	v_fmac_f32_e32 v82, v86, v86
	v_fmac_f32_e32 v83, v84, v84
	v_add_f32_e32 v82, v82, v83
	v_add_f32_e32 v82, v90, v82
	ds_bpermute_b32 v83, v119, v82
	v_lshl_add_u64 v[88:89], v[104:105], 0, v[114:115]
	v_cvt_pk_bf16_f32 v86, v86, v87
	v_cvt_pk_bf16_f32 v87, v84, v85
	v_lshl_add_u64 v[84:85], v[88:89], 1, s[14:15]
	s_waitcnt lgkmcnt(0)
	v_add_f32_e32 v82, v82, v83
	ds_bpermute_b32 v83, v118, v82
	global_store_dwordx2 v[84:85], v[86:87], off
	s_and_saveexec_b64 s[50:51], vcc
	s_cbranch_execz .LBB0_3073
	v_lshlrev_b64 v[84:85], 8, v[98:99]
	v_lshl_add_u64 v[84:85], s[16:17], 0, v[84:85]
	v_lshl_add_u64 v[84:85], s[48:49], 2, v[84:85]
	s_lshl_b32 s12, s66, 2
	v_lshl_add_u64 v[84:85], v[84:85], 0, s[12:13]
	s_waitcnt lgkmcnt(0)
	v_add_f32_e32 v82, v82, v83
	global_store_dword v[84:85], v82, off
.LBB0_3073:
	s_or_b64 exec, exec, s[50:51]
	v_or_b32_e32 v82, 48, v140
	s_waitcnt lgkmcnt(0)
	v_ashrrev_i32_e32 v83, 31, v82
	v_lshlrev_b64 v[88:89], 12, v[82:83]
	v_lshl_add_u64 v[90:91], v[88:89], 0, v[138:139]
	v_lshl_add_u64 v[92:93], v[90:91], 2, s[36:37]
	global_load_dwordx4 v[84:87], v[92:93], off nt
	v_lshl_add_u64 v[90:91], v[90:91], 1, s[14:15]
	s_waitcnt vmcnt(0)
	v_pk_add_f32 v[86:87], v[80:81], v[86:87]
	v_pk_add_f32 v[84:85], v[78:79], v[84:85]
	s_nop 0
	v_cvt_pk_bf16_f32 v78, v84, v85
	v_cvt_pk_bf16_f32 v79, v86, v87
	global_store_dwordx2 v[90:91], v[78:79], off
	global_load_dwordx4 v[78:81], v[92:93], off offset:64 nt
	v_lshl_add_u64 v[90:91], v[88:89], 0, v[126:127]
	v_lshl_add_u64 v[90:91], v[90:91], 1, s[14:15]
	v_mul_f32_e32 v85, v85, v85
	v_mul_f32_e32 v87, v87, v87
	v_fmac_f32_e32 v85, v84, v84
	v_fmac_f32_e32 v87, v86, v86
	v_add_f32_e32 v84, v85, v87
	s_waitcnt vmcnt(0)
	v_pk_add_f32 v[80:81], v[76:77], v[80:81]
	v_pk_add_f32 v[78:79], v[74:75], v[78:79]
	s_nop 0
	v_cvt_pk_bf16_f32 v74, v78, v79
	v_cvt_pk_bf16_f32 v75, v80, v81
	global_store_dwordx2 v[90:91], v[74:75], off
	global_load_dwordx4 v[74:77], v[92:93], off offset:512 nt
	v_lshl_add_u64 v[90:91], v[88:89], 0, v[122:123]
	v_lshl_add_u64 v[90:91], v[90:91], 1, s[14:15]
	v_mul_f32_e32 v79, v79, v79
	v_mul_f32_e32 v81, v81, v81
	v_fmac_f32_e32 v79, v78, v78
	v_fmac_f32_e32 v81, v80, v80
	v_add_f32_e32 v78, v79, v81
	v_add_f32_e32 v78, v84, v78
	s_waitcnt vmcnt(0)
	v_pk_add_f32 v[76:77], v[72:73], v[76:77]
	v_pk_add_f32 v[74:75], v[70:71], v[74:75]
	s_nop 0
	v_cvt_pk_bf16_f32 v70, v74, v75
	v_cvt_pk_bf16_f32 v71, v76, v77
	global_store_dwordx2 v[90:91], v[70:71], off
	global_load_dwordx4 v[70:73], v[92:93], off offset:576 nt
	v_mul_f32_e32 v75, v75, v75
	v_mul_f32_e32 v77, v77, v77
	v_fmac_f32_e32 v75, v74, v74
	v_fmac_f32_e32 v77, v76, v76
	v_add_f32_e32 v74, v75, v77
	v_add_f32_e32 v74, v78, v74
	s_waitcnt vmcnt(0)
	v_pk_add_f32 v[68:69], v[68:69], v[72:73]
	v_pk_add_f32 v[70:71], v[66:67], v[70:71]
	v_mul_f32_e32 v67, v69, v69
	v_mul_f32_e32 v66, v71, v71
	v_fmac_f32_e32 v66, v70, v70
	v_fmac_f32_e32 v67, v68, v68
	v_add_f32_e32 v66, v66, v67
	v_add_f32_e32 v66, v74, v66
	ds_bpermute_b32 v67, v119, v66
	v_lshl_add_u64 v[72:73], v[88:89], 0, v[114:115]
	v_cvt_pk_bf16_f32 v70, v70, v71
	v_cvt_pk_bf16_f32 v71, v68, v69
	v_lshl_add_u64 v[68:69], v[72:73], 1, s[14:15]
	s_waitcnt lgkmcnt(0)
	v_add_f32_e32 v66, v66, v67
	ds_bpermute_b32 v67, v118, v66
	global_store_dwordx2 v[68:69], v[70:71], off
	s_and_saveexec_b64 s[50:51], vcc
	s_cbranch_execz .LBB0_3075
	v_lshlrev_b64 v[68:69], 8, v[82:83]
	v_lshl_add_u64 v[68:69], s[16:17], 0, v[68:69]
	v_lshl_add_u64 v[68:69], s[48:49], 2, v[68:69]
	s_lshl_b32 s12, s66, 2
	v_lshl_add_u64 v[68:69], v[68:69], 0, s[12:13]
	s_waitcnt lgkmcnt(0)
	v_add_f32_e32 v66, v66, v67
	global_store_dword v[68:69], v66, off
; __device__ __forceinline__ int fresh_lane() { int l; asm volatile("v_mbcnt_lo_u32_b32 %0, -1, 0\n\tv_mbcnt_hi_u32_b32 %0, -1, %0" : "=v"(l)); return l; }
; __device__ __forceinline__ unsigned cvt_pk_bf16(float lo, float hi) { unsigned r; asm volatile("v_cvt_pk_bf16_f32 %0, %1, %2" : "=v"(r) : "v"(lo), "v"(hi)); return r; }
;     __device__ __forceinline__ void operator()(const f32x4 (&acc)[2][2][4][2], const Unit& u, int wr, int wc, int fr_, int fq_) const {
;         const int l_ = fresh_lane(), fr = l_ & 15, fq = l_ >> 4;
;         const int row0 = u.pm * BM + wr * 64 + fr, col0 = u.pn * BM + wc * 32 + 4 * fq;
; #pragma unroll
;         for (int ai = 0; ai < 2; ++ai)
; #pragma unroll
;             for (int m = 0; m < 4; ++m) { const size_t r = (size_t)(row0 + ai * HALF + m * 16); float ss = 0.f;
; #pragma unroll
;                 for (int bj = 0; bj < 2; ++bj)
; #pragma unroll
;                     for (int n = 0; n < 2; ++n) { const size_t o = r * ldc + col0 + bj * HALF + n * 16; const f32x4 c = *(const f32x4*)(R + o) + acc[ai][bj][m][n];
;                         ss += (c[0] * c[0] + c[1] * c[1]) + (c[2] * c[2] + c[3] * c[3]);
;                         u32x2 w; w.x = cvt_pk_bf16(c[0], c[1]); w.y = cvt_pk_bf16(c[2], c[3]); *(u32x2*)(HB + o) = w; }
;                 ss += __builtin_bit_cast(float, __builtin_amdgcn_ds_bpermute((l_ ^ 16) << 2, __builtin_bit_cast(int, ss)));
;                 ss += __builtin_bit_cast(float, __builtin_amdgcn_ds_bpermute((l_ ^ 32) << 2, __builtin_bit_cast(int, ss)));
;                 if (fq == 0) PSQ[r * 64 + u.pn * 4 + wc] = ss;
;                 asm volatile("" ::: "memory"); }
.LBB0_3075:
	s_or_b64 exec, exec, s[50:51]
	v_add_u32_e32 v66, 0x80, v140
	s_waitcnt lgkmcnt(0)
	v_ashrrev_i32_e32 v67, 31, v66
	v_lshlrev_b64 v[72:73], 12, v[66:67]
	v_lshl_add_u64 v[74:75], v[72:73], 0, v[138:139]
	v_lshl_add_u64 v[76:77], v[74:75], 2, s[36:37]
	global_load_dwordx4 v[68:71], v[76:77], off nt
	v_lshl_add_u64 v[74:75], v[74:75], 1, s[14:15]
	s_waitcnt vmcnt(0)
	v_pk_add_f32 v[70:71], v[64:65], v[70:71]
	v_pk_add_f32 v[68:69], v[62:63], v[68:69]
	s_nop 0
	v_cvt_pk_bf16_f32 v62, v68, v69
	v_cvt_pk_bf16_f32 v63, v70, v71
	global_store_dwordx2 v[74:75], v[62:63], off
	global_load_dwordx4 v[62:65], v[76:77], off offset:64 nt
	v_lshl_add_u64 v[74:75], v[72:73], 0, v[126:127]
	v_lshl_add_u64 v[74:75], v[74:75], 1, s[14:15]
	v_mul_f32_e32 v69, v69, v69
	v_mul_f32_e32 v71, v71, v71
	v_fmac_f32_e32 v69, v68, v68
	v_fmac_f32_e32 v71, v70, v70
	v_add_f32_e32 v68, v69, v71
	s_waitcnt vmcnt(0)
	v_pk_add_f32 v[64:65], v[60:61], v[64:65]
	v_pk_add_f32 v[62:63], v[58:59], v[62:63]
	s_nop 0
	v_cvt_pk_bf16_f32 v58, v62, v63
	v_cvt_pk_bf16_f32 v59, v64, v65
	global_store_dwordx2 v[74:75], v[58:59], off
	global_load_dwordx4 v[58:61], v[76:77], off offset:512 nt
	v_lshl_add_u64 v[74:75], v[72:73], 0, v[122:123]
	v_lshl_add_u64 v[74:75], v[74:75], 1, s[14:15]
	v_mul_f32_e32 v63, v63, v63
	v_mul_f32_e32 v65, v65, v65
	v_fmac_f32_e32 v63, v62, v62
	v_fmac_f32_e32 v65, v64, v64
	v_add_f32_e32 v62, v63, v65
	v_add_f32_e32 v62, v68, v62
	s_waitcnt vmcnt(0)
	v_pk_add_f32 v[60:61], v[56:57], v[60:61]
	v_pk_add_f32 v[58:59], v[54:55], v[58:59]
	s_nop 0
	v_cvt_pk_bf16_f32 v54, v58, v59
	v_cvt_pk_bf16_f32 v55, v60, v61
	global_store_dwordx2 v[74:75], v[54:55], off
	global_load_dwordx4 v[54:57], v[76:77], off offset:576 nt
	v_mul_f32_e32 v59, v59, v59
	v_mul_f32_e32 v61, v61, v61
	v_fmac_f32_e32 v59, v58, v58
	v_fmac_f32_e32 v61, v60, v60
	v_add_f32_e32 v58, v59, v61
	v_add_f32_e32 v58, v62, v58
	s_waitcnt vmcnt(0)
	v_pk_add_f32 v[52:53], v[52:53], v[56:57]
	v_pk_add_f32 v[54:55], v[50:51], v[54:55]
	v_mul_f32_e32 v51, v53, v53
	v_mul_f32_e32 v50, v55, v55
	v_fmac_f32_e32 v50, v54, v54
	v_fmac_f32_e32 v51, v52, v52
	v_add_f32_e32 v50, v50, v51
	v_add_f32_e32 v50, v58, v50
	ds_bpermute_b32 v51, v119, v50
	v_lshl_add_u64 v[56:57], v[72:73], 0, v[114:115]
	v_cvt_pk_bf16_f32 v54, v54, v55
	v_cvt_pk_bf16_f32 v55, v52, v53
	v_lshl_add_u64 v[52:53], v[56:57], 1, s[14:15]
	s_waitcnt lgkmcnt(0)
	v_add_f32_e32 v50, v50, v51
	ds_bpermute_b32 v51, v118, v50
	global_store_dwordx2 v[52:53], v[54:55], off
	s_and_saveexec_b64 s[50:51], vcc
	s_cbranch_execz .LBB0_3077
	v_lshlrev_b64 v[52:53], 8, v[66:67]
	v_lshl_add_u64 v[52:53], s[16:17], 0, v[52:53]
	v_lshl_add_u64 v[52:53], s[48:49], 2, v[52:53]
	s_lshl_b32 s12, s66, 2
	v_lshl_add_u64 v[52:53], v[52:53], 0, s[12:13]
	s_waitcnt lgkmcnt(0)
	v_add_f32_e32 v50, v50, v51
	global_store_dword v[52:53], v50, off
.LBB0_3077:
	s_or_b64 exec, exec, s[50:51]
	v_add_u32_e32 v50, 0x90, v140
	s_waitcnt lgkmcnt(0)
	v_ashrrev_i32_e32 v51, 31, v50
	v_lshlrev_b64 v[56:57], 12, v[50:51]
	v_lshl_add_u64 v[58:59], v[56:57], 0, v[138:139]
	v_lshl_add_u64 v[60:61], v[58:59], 2, s[36:37]
	global_load_dwordx4 v[52:55], v[60:61], off nt
	v_lshl_add_u64 v[58:59], v[58:59], 1, s[14:15]
	s_waitcnt vmcnt(0)
	v_pk_add_f32 v[54:55], v[48:49], v[54:55]
	v_pk_add_f32 v[52:53], v[46:47], v[52:53]
	s_nop 0
	v_cvt_pk_bf16_f32 v46, v52, v53
	v_cvt_pk_bf16_f32 v47, v54, v55
	global_store_dwordx2 v[58:59], v[46:47], off
	global_load_dwordx4 v[46:49], v[60:61], off offset:64 nt
	v_lshl_add_u64 v[58:59], v[56:57], 0, v[126:127]
	v_lshl_add_u64 v[58:59], v[58:59], 1, s[14:15]
	v_mul_f32_e32 v53, v53, v53
	v_mul_f32_e32 v55, v55, v55
	v_fmac_f32_e32 v53, v52, v52
	v_fmac_f32_e32 v55, v54, v54
	v_add_f32_e32 v52, v53, v55
	s_waitcnt vmcnt(0)
	v_pk_add_f32 v[48:49], v[44:45], v[48:49]
	v_pk_add_f32 v[46:47], v[42:43], v[46:47]
	s_nop 0
	v_cvt_pk_bf16_f32 v42, v46, v47
	v_cvt_pk_bf16_f32 v43, v48, v49
	global_store_dwordx2 v[58:59], v[42:43], off
	global_load_dwordx4 v[42:45], v[60:61], off offset:512 nt
	v_lshl_add_u64 v[58:59], v[56:57], 0, v[122:123]
	v_lshl_add_u64 v[58:59], v[58:59], 1, s[14:15]
	v_mul_f32_e32 v47, v47, v47
	v_mul_f32_e32 v49, v49, v49
	v_fmac_f32_e32 v47, v46, v46
	v_fmac_f32_e32 v49, v48, v48
	v_add_f32_e32 v46, v47, v49
	v_add_f32_e32 v46, v52, v46
	s_waitcnt vmcnt(0)
	v_pk_add_f32 v[44:45], v[40:41], v[44:45]
	v_pk_add_f32 v[42:43], v[38:39], v[42:43]
	s_nop 0
	v_cvt_pk_bf16_f32 v38, v42, v43
	v_cvt_pk_bf16_f32 v39, v44, v45
	global_store_dwordx2 v[58:59], v[38:39], off
	global_load_dwordx4 v[38:41], v[60:61], off offset:576 nt
	v_mul_f32_e32 v43, v43, v43
	v_mul_f32_e32 v45, v45, v45
	v_fmac_f32_e32 v43, v42, v42
	v_fmac_f32_e32 v45, v44, v44
	v_add_f32_e32 v42, v43, v45
	v_add_f32_e32 v42, v46, v42
	s_waitcnt vmcnt(0)
	v_pk_add_f32 v[36:37], v[36:37], v[40:41]
	v_pk_add_f32 v[38:39], v[34:35], v[38:39]
	v_mul_f32_e32 v35, v37, v37
	v_mul_f32_e32 v34, v39, v39
	v_fmac_f32_e32 v34, v38, v38
	v_fmac_f32_e32 v35, v36, v36
	v_add_f32_e32 v34, v34, v35
	v_add_f32_e32 v34, v42, v34
	ds_bpermute_b32 v35, v119, v34
	v_lshl_add_u64 v[40:41], v[56:57], 0, v[114:115]
	v_cvt_pk_bf16_f32 v38, v38, v39
	v_cvt_pk_bf16_f32 v39, v36, v37
	v_lshl_add_u64 v[36:37], v[40:41], 1, s[14:15]
	s_waitcnt lgkmcnt(0)
	v_add_f32_e32 v34, v34, v35
	ds_bpermute_b32 v35, v118, v34
	global_store_dwordx2 v[36:37], v[38:39], off
	s_and_saveexec_b64 s[50:51], vcc
	s_cbranch_execz .LBB0_3079
	v_lshlrev_b64 v[36:37], 8, v[50:51]
	v_lshl_add_u64 v[36:37], s[16:17], 0, v[36:37]
	v_lshl_add_u64 v[36:37], s[48:49], 2, v[36:37]
	s_lshl_b32 s12, s66, 2
	v_lshl_add_u64 v[36:37], v[36:37], 0, s[12:13]
	s_waitcnt lgkmcnt(0)
	v_add_f32_e32 v34, v34, v35
	global_store_dword v[36:37], v34, off
; __device__ __forceinline__ int fresh_lane() { int l; asm volatile("v_mbcnt_lo_u32_b32 %0, -1, 0\n\tv_mbcnt_hi_u32_b32 %0, -1, %0" : "=v"(l)); return l; }
; __device__ __forceinline__ unsigned cvt_pk_bf16(float lo, float hi) { unsigned r; asm volatile("v_cvt_pk_bf16_f32 %0, %1, %2" : "=v"(r) : "v"(lo), "v"(hi)); return r; }
;     __device__ __forceinline__ void operator()(const f32x4 (&acc)[2][2][4][2], const Unit& u, int wr, int wc, int fr_, int fq_) const {
;         const int l_ = fresh_lane(), fr = l_ & 15, fq = l_ >> 4;
;         const int row0 = u.pm * BM + wr * 64 + fr, col0 = u.pn * BM + wc * 32 + 4 * fq;
; #pragma unroll
;         for (int ai = 0; ai < 2; ++ai)
; #pragma unroll
;             for (int m = 0; m < 4; ++m) { const size_t r = (size_t)(row0 + ai * HALF + m * 16); float ss = 0.f;
; #pragma unroll
;                 for (int bj = 0; bj < 2; ++bj)
; #pragma unroll
;                     for (int n = 0; n < 2; ++n) { const size_t o = r * ldc + col0 + bj * HALF + n * 16; const f32x4 c = *(const f32x4*)(R + o) + acc[ai][bj][m][n];
;                         ss += (c[0] * c[0] + c[1] * c[1]) + (c[2] * c[2] + c[3] * c[3]);
;                         u32x2 w; w.x = cvt_pk_bf16(c[0], c[1]); w.y = cvt_pk_bf16(c[2], c[3]); *(u32x2*)(HB + o) = w; }
;                 ss += __builtin_bit_cast(float, __builtin_amdgcn_ds_bpermute((l_ ^ 16) << 2, __builtin_bit_cast(int, ss)));
;                 ss += __builtin_bit_cast(float, __builtin_amdgcn_ds_bpermute((l_ ^ 32) << 2, __builtin_bit_cast(int, ss)));
;                 if (fq == 0) PSQ[r * 64 + u.pn * 4 + wc] = ss;
;                 asm volatile("" ::: "memory"); }
.LBB0_3079:
	s_or_b64 exec, exec, s[50:51]
	v_add_u32_e32 v34, 0xa0, v140
	s_waitcnt lgkmcnt(0)
	v_ashrrev_i32_e32 v35, 31, v34
	v_lshlrev_b64 v[40:41], 12, v[34:35]
	v_lshl_add_u64 v[42:43], v[40:41], 0, v[138:139]
	v_lshl_add_u64 v[44:45], v[42:43], 2, s[36:37]
	global_load_dwordx4 v[36:39], v[44:45], off nt
	v_lshl_add_u64 v[42:43], v[42:43], 1, s[14:15]
	s_waitcnt vmcnt(0)
	v_pk_add_f32 v[38:39], v[32:33], v[38:39]
	v_pk_add_f32 v[36:37], v[30:31], v[36:37]
	s_nop 0
	v_cvt_pk_bf16_f32 v30, v36, v37
	v_cvt_pk_bf16_f32 v31, v38, v39
	global_store_dwordx2 v[42:43], v[30:31], off
	global_load_dwordx4 v[30:33], v[44:45], off offset:64 nt
	v_lshl_add_u64 v[42:43], v[40:41], 0, v[126:127]
	v_lshl_add_u64 v[42:43], v[42:43], 1, s[14:15]
	v_mul_f32_e32 v37, v37, v37
	v_mul_f32_e32 v39, v39, v39
	v_fmac_f32_e32 v37, v36, v36
	v_fmac_f32_e32 v39, v38, v38
	v_add_f32_e32 v36, v37, v39
	s_waitcnt vmcnt(0)
	v_pk_add_f32 v[32:33], v[28:29], v[32:33]
	v_pk_add_f32 v[30:31], v[26:27], v[30:31]
	s_nop 0
	v_cvt_pk_bf16_f32 v26, v30, v31
	v_cvt_pk_bf16_f32 v27, v32, v33
	global_store_dwordx2 v[42:43], v[26:27], off
	global_load_dwordx4 v[26:29], v[44:45], off offset:512 nt
	v_lshl_add_u64 v[42:43], v[40:41], 0, v[122:123]
	v_lshl_add_u64 v[42:43], v[42:43], 1, s[14:15]
	v_mul_f32_e32 v31, v31, v31
	v_mul_f32_e32 v33, v33, v33
	v_fmac_f32_e32 v31, v30, v30
	v_fmac_f32_e32 v33, v32, v32
	v_add_f32_e32 v30, v31, v33
	v_add_f32_e32 v30, v36, v30
	s_waitcnt vmcnt(0)
	v_pk_add_f32 v[28:29], v[24:25], v[28:29]
	v_pk_add_f32 v[26:27], v[22:23], v[26:27]
	s_nop 0
	v_cvt_pk_bf16_f32 v22, v26, v27
	v_cvt_pk_bf16_f32 v23, v28, v29
	global_store_dwordx2 v[42:43], v[22:23], off
	global_load_dwordx4 v[22:25], v[44:45], off offset:576 nt
	v_mul_f32_e32 v27, v27, v27
	v_mul_f32_e32 v29, v29, v29
	v_fmac_f32_e32 v27, v26, v26
	v_fmac_f32_e32 v29, v28, v28
	v_add_f32_e32 v26, v27, v29
	v_add_f32_e32 v26, v30, v26
	s_waitcnt vmcnt(0)
	v_pk_add_f32 v[20:21], v[20:21], v[24:25]
	v_pk_add_f32 v[22:23], v[18:19], v[22:23]
	v_mul_f32_e32 v19, v21, v21
	v_mul_f32_e32 v18, v23, v23
	v_fmac_f32_e32 v18, v22, v22
	v_fmac_f32_e32 v19, v20, v20
	v_add_f32_e32 v18, v18, v19
	v_add_f32_e32 v18, v26, v18
	ds_bpermute_b32 v19, v119, v18
	v_lshl_add_u64 v[24:25], v[40:41], 0, v[114:115]
	v_cvt_pk_bf16_f32 v22, v22, v23
	v_cvt_pk_bf16_f32 v23, v20, v21
	v_lshl_add_u64 v[20:21], v[24:25], 1, s[14:15]
	s_waitcnt lgkmcnt(0)
	v_add_f32_e32 v18, v18, v19
	ds_bpermute_b32 v19, v118, v18
	global_store_dwordx2 v[20:21], v[22:23], off
	s_and_saveexec_b64 s[50:51], vcc
	s_cbranch_execz .LBB0_3081
	v_lshlrev_b64 v[20:21], 8, v[34:35]
	v_lshl_add_u64 v[20:21], s[16:17], 0, v[20:21]
	v_lshl_add_u64 v[20:21], s[48:49], 2, v[20:21]
	s_lshl_b32 s12, s66, 2
	v_lshl_add_u64 v[20:21], v[20:21], 0, s[12:13]
	s_waitcnt lgkmcnt(0)
	v_add_f32_e32 v18, v18, v19
	global_store_dword v[20:21], v18, off
.LBB0_3081:
	s_or_b64 exec, exec, s[50:51]
	v_add_u32_e32 v18, 0xb0, v140
	s_waitcnt lgkmcnt(0)
	v_ashrrev_i32_e32 v19, 31, v18
	v_lshlrev_b64 v[24:25], 12, v[18:19]
	v_lshl_add_u64 v[26:27], v[24:25], 0, v[138:139]
	v_lshl_add_u64 v[28:29], v[26:27], 2, s[36:37]
	global_load_dwordx4 v[20:23], v[28:29], off nt
	v_lshl_add_u64 v[26:27], v[26:27], 1, s[14:15]
	s_waitcnt vmcnt(0)
	v_pk_add_f32 v[22:23], v[16:17], v[22:23]
	v_pk_add_f32 v[20:21], v[14:15], v[20:21]
	s_nop 0
	v_cvt_pk_bf16_f32 v14, v20, v21
	v_cvt_pk_bf16_f32 v15, v22, v23
	global_store_dwordx2 v[26:27], v[14:15], off
	global_load_dwordx4 v[14:17], v[28:29], off offset:64 nt
	v_lshl_add_u64 v[26:27], v[24:25], 0, v[126:127]
	v_lshl_add_u64 v[26:27], v[26:27], 1, s[14:15]
	v_mul_f32_e32 v21, v21, v21
	v_mul_f32_e32 v23, v23, v23
	v_fmac_f32_e32 v21, v20, v20
	v_fmac_f32_e32 v23, v22, v22
	v_add_f32_e32 v20, v21, v23
	s_waitcnt vmcnt(0)
	v_pk_add_f32 v[16:17], v[12:13], v[16:17]
	v_pk_add_f32 v[14:15], v[10:11], v[14:15]
	s_nop 0
	v_cvt_pk_bf16_f32 v10, v14, v15
	v_cvt_pk_bf16_f32 v11, v16, v17
	global_store_dwordx2 v[26:27], v[10:11], off
	global_load_dwordx4 v[10:13], v[28:29], off offset:512 nt
	v_lshl_add_u64 v[26:27], v[24:25], 0, v[122:123]
	v_lshl_add_u64 v[26:27], v[26:27], 1, s[14:15]
	v_mul_f32_e32 v15, v15, v15
	v_mul_f32_e32 v17, v17, v17
	v_fmac_f32_e32 v15, v14, v14
	v_fmac_f32_e32 v17, v16, v16
	v_add_f32_e32 v14, v15, v17
	v_add_f32_e32 v14, v20, v14
	s_waitcnt vmcnt(0)
	v_pk_add_f32 v[12:13], v[8:9], v[12:13]
	v_pk_add_f32 v[10:11], v[6:7], v[10:11]
	s_nop 0
	v_cvt_pk_bf16_f32 v6, v10, v11
	v_cvt_pk_bf16_f32 v7, v12, v13
	global_store_dwordx2 v[26:27], v[6:7], off
	global_load_dwordx4 v[6:9], v[28:29], off offset:576 nt
	v_mul_f32_e32 v11, v11, v11
	v_mul_f32_e32 v13, v13, v13
	v_fmac_f32_e32 v11, v10, v10
	v_fmac_f32_e32 v13, v12, v12
	v_add_f32_e32 v10, v11, v13
	v_add_f32_e32 v10, v14, v10
	s_waitcnt vmcnt(0)
	v_pk_add_f32 v[4:5], v[4:5], v[8:9]
	v_pk_add_f32 v[6:7], v[2:3], v[6:7]
	v_mul_f32_e32 v3, v5, v5
	v_mul_f32_e32 v2, v7, v7
	v_fmac_f32_e32 v2, v6, v6
	v_fmac_f32_e32 v3, v4, v4
	v_add_f32_e32 v2, v2, v3
	v_add_f32_e32 v2, v10, v2
	ds_bpermute_b32 v3, v119, v2
	v_lshl_add_u64 v[8:9], v[24:25], 0, v[114:115]
	v_cvt_pk_bf16_f32 v6, v6, v7
	v_cvt_pk_bf16_f32 v7, v4, v5
	v_lshl_add_u64 v[4:5], v[8:9], 1, s[14:15]
	s_waitcnt lgkmcnt(0)
	v_add_f32_e32 v2, v2, v3
	ds_bpermute_b32 v3, v118, v2
	global_store_dwordx2 v[4:5], v[6:7], off
	s_and_saveexec_b64 s[50:51], vcc
	s_cbranch_execz .LBB0_3083
	v_lshlrev_b64 v[4:5], 8, v[18:19]
	v_lshl_add_u64 v[4:5], s[16:17], 0, v[4:5]
	v_lshl_add_u64 v[4:5], s[48:49], 2, v[4:5]
	s_lshl_b32 s12, s66, 2
	v_lshl_add_u64 v[4:5], v[4:5], 0, s[12:13]
	s_waitcnt lgkmcnt(0)
	v_add_f32_e32 v2, v2, v3
	global_store_dword v[4:5], v2, off
